# speedup vs baseline: 1.0192x; 1.0051x over previous
_Z12scan2_kernelPKDF16_S0_S0_S0_S0_PKfS2_S2_S2_PDF16_PfS4_:
	s_and_b32 s3, s2, 7
	s_lshr_b32 s2, s2, 3
	s_lshl_b32 s3, s3, 5
	s_or_b32 s2, s2, s3
	s_load_dwordx8 s[4:11], s[0:1], 0x0
	s_load_dwordx8 s[12:19], s[0:1], 0x20
	s_load_dwordx4 s[20:23], s[0:1], 0x40
	s_load_dwordx2 s[24:25], s[0:1], 0x50
	s_and_b32 s26, s2, 3
	s_bfe_u32 s27, s2, 0x50002
	s_lshr_b32 s28, s2, 7
	s_lshl_b32 s29, s26, 3
	v_lshrrev_b32_e32 v1, 6, v0
	v_and_b32_e32 v2, 15, v0
	v_bfe_u32 v3, v0, 4, 2
	v_and_b32_e32 v42, 63, v0
	v_readfirstlane_b32 s40, v1
	v_mov_b32_e32 v43, v0
	v_lshrrev_b32_e32 v14, 4, v43
	v_and_b32_e32 v15, 15, v43
	v_and_b32_e32 v188, 15, v14
	v_xor_b32_e32 v15, v15, v188
	v_lshlrev_b32_e32 v15, 4, v15
	v_lshl_or_b32 v4, v14, 13, v15
	v_lshl_or_b32 v6, v14, 8, v15
	v_lshrrev_b32_e32 v14, 3, v43
	v_and_b32_e32 v15, 7, v43
	v_and_b32_e32 v188, 7, v14
	v_xor_b32_e32 v15, v15, v188
	v_lshlrev_b32_e32 v15, 4, v15
	v_lshl_or_b32 v8, v14, 12, v15
	v_lshlrev_b32_e32 v40, 4, v43
	v_add_u32_e32 v32, 0xc800, v40
	v_add_u32_e32 v34, 0x19000, v40
	v_add_u32_e32 v43, 0x200, v0
	v_lshrrev_b32_e32 v14, 4, v43
	v_and_b32_e32 v15, 15, v43
	v_and_b32_e32 v188, 15, v14
	v_xor_b32_e32 v15, v15, v188
	v_lshlrev_b32_e32 v15, 4, v15
	v_lshl_or_b32 v5, v14, 13, v15
	v_lshl_or_b32 v7, v14, 8, v15
	v_lshrrev_b32_e32 v14, 3, v43
	v_and_b32_e32 v15, 7, v43
	v_and_b32_e32 v188, 7, v14
	v_xor_b32_e32 v15, v15, v188
	v_lshlrev_b32_e32 v15, 4, v15
	v_lshl_or_b32 v9, v14, 12, v15
	v_lshlrev_b32_e32 v41, 4, v43
	v_add_u32_e32 v33, 0xc800, v41
	v_add_u32_e32 v35, 0x19000, v41
	s_sub_u32 s45, 11, s40
	s_cmp_lt_u32 s40, 4
	s_cselect_b32 s41, s40, s45
	s_lshr_b32 s42, s41, 1
	s_lshl_b32 s43, s40, 10
	s_lshl_b32 s44, s40, 8
	s_and_b32 s45, s40, 1
	s_lshl_b32 s45, s45, 8
	v_lshl_add_u32 v10, v42, 2, s45
	s_lshl_b32 s45, s41, 4
	v_add_u32_e32 v14, s45, v2
	v_add_u32_e32 v15, 0, v3
	v_xor_b32_e32 v15, v15, v2
	v_lshlrev_b32_e32 v15, 4, v15
	v_lshl_or_b32 v16, v2, 8, v15
	v_add_u32_e32 v20, 0xc800, v16
	v_add_u32_e32 v212, 0x19000, v16
	v_add_u32_e32 v15, 4, v3
	v_xor_b32_e32 v15, v15, v2
	v_lshlrev_b32_e32 v15, 4, v15
	v_lshl_or_b32 v17, v2, 8, v15
	v_add_u32_e32 v21, 0xc800, v17
	v_add_u32_e32 v213, 0x19000, v17
	v_add_u32_e32 v15, 8, v3
	v_xor_b32_e32 v15, v15, v2
	v_lshlrev_b32_e32 v15, 4, v15
	v_lshl_or_b32 v18, v2, 8, v15
	v_add_u32_e32 v22, 0xc800, v18
	v_add_u32_e32 v214, 0x19000, v18
	v_add_u32_e32 v15, 12, v3
	v_xor_b32_e32 v15, v15, v2
	v_lshlrev_b32_e32 v15, 4, v15
	v_lshl_or_b32 v19, v2, 8, v15
	v_add_u32_e32 v23, 0xc800, v19
	v_add_u32_e32 v215, 0x19000, v19
	v_lshrrev_b32_e32 v188, 1, v3
	v_and_b32_e32 v189, 7, v14
	v_and_b32_e32 v190, 1, v3
	v_lshlrev_b32_e32 v190, 3, v190
	v_lshl_or_b32 v190, v14, 7, v190
	v_add_u32_e32 v15, 0, v188
	v_xor_b32_e32 v15, v15, v189
	v_lshl_add_u32 v24, v15, 4, v190
	v_add_u32_e32 v28, 0xc800, v24
	v_add_u32_e32 v216, 0x19000, v24
	v_add_u32_e32 v15, 2, v188
	v_xor_b32_e32 v15, v15, v189
	v_lshl_add_u32 v25, v15, 4, v190
	v_add_u32_e32 v29, 0xc800, v25
	v_add_u32_e32 v217, 0x19000, v25
	v_add_u32_e32 v15, 4, v188
	v_xor_b32_e32 v15, v15, v189
	v_lshl_add_u32 v26, v15, 4, v190
	v_add_u32_e32 v30, 0xc800, v26
	v_add_u32_e32 v218, 0x19000, v26
	v_add_u32_e32 v15, 6, v188
	v_xor_b32_e32 v15, v15, v189
	v_lshl_add_u32 v27, v15, 4, v190
	v_add_u32_e32 v31, 0xc800, v27
	v_add_u32_e32 v219, 0x19000, v27
	v_lshlrev_b32_e32 v242, 12, v14
	v_lshl_add_u32 v242, v3, 3, v242
	v_lshlrev_b32_e32 v36, 2, v14
	v_add_u32_e32 v37, 0xc800, v36
	v_add_u32_e32 v220, 0x19000, v36
	v_lshlrev_b32_e32 v38, 5, v3
	v_add_u32_e32 v39, 0xc800, v38
	v_add_u32_e32 v221, 0x19000, v38
	s_and_b32 s45, s41, 1
	s_lshl_b32 s45, s45, 4
	v_add_u32_e32 v43, s45, v2
	v_lshlrev_b32_e32 v189, 3, v3
	v_sub_u32_e32 v43, v43, v189
	v_cmp_le_i32_e64 s[52:53], 0, v43
	v_cmp_le_i32_e64 s[54:55], 1, v43
	v_cmp_le_i32_e64 s[56:57], 2, v43
	v_cmp_le_i32_e64 s[58:59], 3, v43
	v_cmp_le_i32_e64 s[60:61], 4, v43
	v_cmp_le_i32_e64 s[62:63], 5, v43
	v_cmp_le_i32_e64 s[64:65], 6, v43
	v_cmp_le_i32_e64 s[66:67], 7, v43
	v_cmp_eq_u32_e32 vcc, 0, v43
	s_nop 1
	v_cndmask_b32_e64 v188, 0, 1.0, vcc
	v_cmp_eq_u32_e32 vcc, 1, v43
	s_nop 1
	v_cndmask_b32_e64 v189, 0, 1.0, vcc
	v_cmp_eq_u32_e32 vcc, 2, v43
	s_nop 1
	v_cndmask_b32_e64 v190, 0, 1.0, vcc
	v_cmp_eq_u32_e32 vcc, 3, v43
	s_nop 1
	v_cndmask_b32_e64 v191, 0, 1.0, vcc
	v_cmp_eq_u32_e32 vcc, 4, v43
	s_nop 1
	v_cndmask_b32_e64 v192, 0, 1.0, vcc
	v_cmp_eq_u32_e32 vcc, 5, v43
	s_nop 1
	v_cndmask_b32_e64 v193, 0, 1.0, vcc
	v_cmp_eq_u32_e32 vcc, 6, v43
	s_nop 1
	v_cndmask_b32_e64 v194, 0, 1.0, vcc
	v_cmp_eq_u32_e32 vcc, 7, v43
	s_nop 1
	v_cndmask_b32_e64 v195, 0, 1.0, vcc
	v_cvt_pk_f16_f32 v92, v188, v189
	v_cvt_pk_f16_f32 v93, v190, v191
	v_cvt_pk_f16_f32 v94, v192, v193
	v_cvt_pk_f16_f32 v95, v194, v195
	v_mov_b32_e32 v250, 0
	v_mov_b32_e32 v251, 0
	s_waitcnt lgkmcnt(0)
	s_lshl_b32 s45, s28, 12
	s_lshl_b32 s48, s27, 7
	s_add_u32 s45, s45, s48
	s_lshl_b32 s48, s45, 9
	s_add_u32 s48, s4, s48
	s_addc_u32 s49, s5, 0
	v_lshlrev_b32_e32 v188, 9, v14
	v_lshl_add_u32 v188, v3, 4, v188
	global_load_dwordx4 v[44:47], v188, s[48:49] offset:256
	global_load_dwordx4 v[48:51], v188, s[48:49] offset:320
	global_load_dwordx4 v[52:55], v188, s[48:49] offset:384
	global_load_dwordx4 v[56:59], v188, s[48:49] offset:448
	s_lshl_b32 s48, s28, 5
	s_add_u32 s48, s48, s27
	s_lshl_b32 s48, s48, 15
	s_add_u32 s48, s10, s48
	s_addc_u32 s49, s11, 0
	v_lshlrev_b32_e32 v188, 8, v14
	v_lshl_add_u32 v188, v3, 4, v188
	global_load_dwordx4 v[144:147], v188, s[48:49] offset:0
	global_load_dwordx4 v[148:151], v188, s[48:49] offset:64
	global_load_dwordx4 v[152:155], v188, s[48:49] offset:128
	global_load_dwordx4 v[156:159], v188, s[48:49] offset:192
	v_and_b32_e32 v188, 7, v42
	v_add_u32_e32 v188, s29, v188
	v_lshlrev_b32_e32 v188, 2, v188
	global_load_dword v11, v188, s[20:21]
	global_load_dword v12, v188, s[18:19]
	s_mul_i32 s48, s28, 0x900
	s_lshl_b32 s49, s29, 6
	s_add_u32 s48, s48, s49
	s_lshl_b32 s48, s48, 13
	s_lshl_b32 s49, s27, 8
	s_add_u32 s48, s48, s49
	s_add_u32 s30, s6, s48
	s_addc_u32 s31, s7, 0
	s_lshl_b32 s48, s28, 5
	s_add_u32 s48, s48, s27
	s_lshl_b32 s48, s48, 5
	s_add_u32 s48, s48, s29
	s_lshl_b32 s48, s48, 14
	s_add_u32 s32, s12, s48
	s_addc_u32 s33, s13, 0
	s_lshl_b32 s48, s45, 12
	s_lshl_b32 s49, s29, 7
	s_add_u32 s48, s48, s49
	s_add_u32 s34, s8, s48
	s_addc_u32 s35, s9, 0
	s_add_u32 s38, s22, s48
	s_addc_u32 s39, s23, 0
	s_lshl_b32 s48, s28, 5
	s_add_u32 s48, s48, s29
	s_lshl_b32 s48, s48, 14
	s_lshl_b32 s49, s27, 9
	s_add_u32 s48, s48, s49
	s_lshr_b32 s49, s40, 1
	s_cmp_eq_u32 s49, 1
	s_cselect_b32 s50, s14, s16
	s_cselect_b32 s51, s15, s17
	s_add_u32 s36, s50, s48
	s_addc_u32 s37, s51, 0
	s_lshl_b32 s48, s45, 2
	s_add_u32 s24, s24, s48
	s_addc_u32 s25, s25, 0
	v_lshlrev_b32_e32 v15, 2, v14
	s_mov_b32 s51, 0xbfb8aa3b
	s_mov_b32 s50, 0x41800000
	s_add_u32 m0, s43, 0x0
	s_nop 0
	global_load_lds_dwordx4 v4, s[30:31]
	s_add_u32 m0, s43, 0x4000
	s_nop 0
	global_load_lds_dwordx4 v6, s[32:33]
	s_add_u32 m0, s43, 0x8000
	s_nop 0
	global_load_lds_dwordx4 v8, s[34:35]
	s_add_u32 m0, s43, 0x2000
	s_nop 0
	global_load_lds_dwordx4 v5, s[30:31]
	s_add_u32 m0, s43, 0x6000
	s_nop 0
	global_load_lds_dwordx4 v7, s[32:33]
	s_add_u32 m0, s43, 0xa000
	s_nop 0
	global_load_lds_dwordx4 v9, s[34:35]
	s_add_u32 m0, s44, 0xc000
	s_nop 0
	global_load_lds_dword v10, s[36:37]
	s_add_u32 s30, s30, 0x80000
	s_addc_u32 s31, s31, 0
	s_add_u32 s32, s32, 0x4000
	s_addc_u32 s33, s33, 0
	s_add_u32 s34, s34, 0x80
	s_addc_u32 s35, s35, 0
	s_add_u32 s36, s36, 0x4000
	s_addc_u32 s37, s37, 0
	s_add_u32 m0, s43, 0xc800
	s_nop 0
	global_load_lds_dwordx4 v4, s[30:31]
	s_add_u32 m0, s43, 0x10800
	s_nop 0
	global_load_lds_dwordx4 v6, s[32:33]
	s_add_u32 m0, s43, 0x14800
	s_nop 0
	global_load_lds_dwordx4 v8, s[34:35]
	s_add_u32 m0, s43, 0xe800
	s_nop 0
	global_load_lds_dwordx4 v5, s[30:31]
	s_add_u32 m0, s43, 0x12800
	s_nop 0
	global_load_lds_dwordx4 v7, s[32:33]
	s_add_u32 m0, s43, 0x16800
	s_nop 0
	global_load_lds_dwordx4 v9, s[34:35]
	s_add_u32 m0, s44, 0x18800
	s_nop 0
	global_load_lds_dword v10, s[36:37]
	s_add_u32 s30, s30, 0x80000
	s_addc_u32 s31, s31, 0
	s_add_u32 s32, s32, 0x4000
	s_addc_u32 s33, s33, 0
	s_add_u32 s34, s34, 0x80
	s_addc_u32 s35, s35, 0
	s_add_u32 s36, s36, 0x4000
	s_addc_u32 s37, s37, 0
	s_waitcnt vmcnt(19)
	v_cvt_f32_f16_e32 v60, v144
	v_cvt_f32_f16_sdwa v61, v144 dst_sel:DWORD dst_unused:UNUSED_PAD src0_sel:WORD_1
	v_cvt_f32_f16_e32 v62, v145
	v_cvt_f32_f16_sdwa v63, v145 dst_sel:DWORD dst_unused:UNUSED_PAD src0_sel:WORD_1
	v_cvt_f32_f16_e32 v64, v146
	v_cvt_f32_f16_sdwa v65, v146 dst_sel:DWORD dst_unused:UNUSED_PAD src0_sel:WORD_1
	v_cvt_f32_f16_e32 v66, v147
	v_cvt_f32_f16_sdwa v67, v147 dst_sel:DWORD dst_unused:UNUSED_PAD src0_sel:WORD_1
	s_waitcnt vmcnt(18)
	v_cvt_f32_f16_e32 v68, v148
	v_cvt_f32_f16_sdwa v69, v148 dst_sel:DWORD dst_unused:UNUSED_PAD src0_sel:WORD_1
	v_cvt_f32_f16_e32 v70, v149
	v_cvt_f32_f16_sdwa v71, v149 dst_sel:DWORD dst_unused:UNUSED_PAD src0_sel:WORD_1
	v_cvt_f32_f16_e32 v72, v150
	v_cvt_f32_f16_sdwa v73, v150 dst_sel:DWORD dst_unused:UNUSED_PAD src0_sel:WORD_1
	v_cvt_f32_f16_e32 v74, v151
	v_cvt_f32_f16_sdwa v75, v151 dst_sel:DWORD dst_unused:UNUSED_PAD src0_sel:WORD_1
	s_waitcnt vmcnt(17)
	v_cvt_f32_f16_e32 v76, v152
	v_cvt_f32_f16_sdwa v77, v152 dst_sel:DWORD dst_unused:UNUSED_PAD src0_sel:WORD_1
	v_cvt_f32_f16_e32 v78, v153
	v_cvt_f32_f16_sdwa v79, v153 dst_sel:DWORD dst_unused:UNUSED_PAD src0_sel:WORD_1
	v_cvt_f32_f16_e32 v80, v154
	v_cvt_f32_f16_sdwa v81, v154 dst_sel:DWORD dst_unused:UNUSED_PAD src0_sel:WORD_1
	v_cvt_f32_f16_e32 v82, v155
	v_cvt_f32_f16_sdwa v83, v155 dst_sel:DWORD dst_unused:UNUSED_PAD src0_sel:WORD_1
	s_waitcnt vmcnt(16)
	v_cvt_f32_f16_e32 v84, v156
	v_cvt_f32_f16_sdwa v85, v156 dst_sel:DWORD dst_unused:UNUSED_PAD src0_sel:WORD_1
	v_cvt_f32_f16_e32 v86, v157
	v_cvt_f32_f16_sdwa v87, v157 dst_sel:DWORD dst_unused:UNUSED_PAD src0_sel:WORD_1
	v_cvt_f32_f16_e32 v88, v158
	v_cvt_f32_f16_sdwa v89, v158 dst_sel:DWORD dst_unused:UNUSED_PAD src0_sel:WORD_1
	v_cvt_f32_f16_e32 v90, v159
	v_cvt_f32_f16_sdwa v91, v159 dst_sel:DWORD dst_unused:UNUSED_PAD src0_sel:WORD_1
	s_waitcnt vmcnt(14)
	s_waitcnt vmcnt(15)
	v_mul_f32_e32 v11, 0x41800000, v11
	s_mov_b32 s48, 0
.Lmy_s2_heads1:
	s_waitcnt vmcnt(7)
	s_add_u32 s49, s48, 0
	s_waitcnt lgkmcnt(0)
	s_barrier
	ds_read_b128 v[144:147], v16 offset:16384
	ds_read_b128 v[148:151], v16 offset:20480
	ds_read_b128 v[152:155], v16 offset:24576
	ds_read_b128 v[156:159], v16 offset:28672
	ds_read_b32 v189, v36 offset:49152
	s_add_u32 m0, s43, 0x19000
	s_nop 0
	global_load_lds_dwordx4 v4, s[30:31]
	s_add_u32 m0, s43, 0x1d000
	s_nop 0
	global_load_lds_dwordx4 v6, s[32:33]
	s_add_u32 m0, s43, 0x21000
	s_nop 0
	global_load_lds_dwordx4 v8, s[34:35]
	s_add_u32 m0, s43, 0x1b000
	s_nop 0
	global_load_lds_dwordx4 v5, s[30:31]
	s_add_u32 m0, s43, 0x1f000
	s_nop 0
	global_load_lds_dwordx4 v7, s[32:33]
	s_add_u32 m0, s43, 0x23000
	s_nop 0
	global_load_lds_dwordx4 v9, s[34:35]
	s_add_u32 m0, s44, 0x25000
	s_nop 0
	global_load_lds_dword v10, s[36:37]
	s_add_u32 s30, s30, 0x80000
	s_addc_u32 s31, s31, 0
	s_add_u32 s32, s32, 0x4000
	s_addc_u32 s33, s33, 0
	s_add_u32 s34, s34, 0x80
	s_addc_u32 s35, s35, 0
	s_add_u32 s36, s36, 0x4000
	s_addc_u32 s37, s37, 0
	ds_read_b128 v[160:163], v17 offset:16384
	ds_read_b128 v[164:167], v17 offset:20480
	ds_read_b128 v[168:171], v17 offset:24576
	ds_read_b128 v[172:175], v17 offset:28672
	s_waitcnt lgkmcnt(4)
	v_mfma_f32_16x16x32_f16 v[96:99], v[144:147], v[44:47], 0
	v_mfma_f32_16x16x32_f16 v[100:103], v[148:151], v[44:47], 0
	v_mfma_f32_16x16x32_f16 v[104:107], v[152:155], v[44:47], 0
	v_mfma_f32_16x16x32_f16 v[108:111], v[156:159], v[44:47], 0
	ds_read_b128 v[144:147], v18 offset:16384
	ds_read_b128 v[148:151], v18 offset:20480
	ds_read_b128 v[152:155], v18 offset:24576
	ds_read_b128 v[156:159], v18 offset:28672
	s_waitcnt lgkmcnt(4)
	v_mfma_f32_16x16x32_f16 v[96:99], v[160:163], v[48:51], v[96:99]
	v_mfma_f32_16x16x32_f16 v[100:103], v[164:167], v[48:51], v[100:103]
	v_mfma_f32_16x16x32_f16 v[104:107], v[168:171], v[48:51], v[104:107]
	v_mfma_f32_16x16x32_f16 v[108:111], v[172:175], v[48:51], v[108:111]
	ds_read_b128 v[160:163], v19 offset:16384
	ds_read_b128 v[164:167], v19 offset:20480
	ds_read_b128 v[168:171], v19 offset:24576
	ds_read_b128 v[172:175], v19 offset:28672
	s_waitcnt lgkmcnt(4)
	v_mfma_f32_16x16x32_f16 v[96:99], v[144:147], v[52:55], v[96:99]
	v_mfma_f32_16x16x32_f16 v[100:103], v[148:151], v[52:55], v[100:103]
	v_mfma_f32_16x16x32_f16 v[104:107], v[152:155], v[52:55], v[104:107]
	v_mfma_f32_16x16x32_f16 v[108:111], v[156:159], v[52:55], v[108:111]
	ds_read_b128 v[176:179], v38 offset:49664
	ds_read_b128 v[180:183], v38 offset:49680
	ds_read_b32 v188, v38 offset:49152
	ds_read_b128 v[144:147], v16 offset:0
	ds_read_b128 v[148:151], v16 offset:4096
	ds_read_b128 v[152:155], v16 offset:8192
	ds_read_b128 v[156:159], v16 offset:12288
	s_waitcnt lgkmcnt(7)
	v_mfma_f32_16x16x32_f16 v[96:99], v[160:163], v[56:59], v[96:99]
	v_mfma_f32_16x16x32_f16 v[100:103], v[164:167], v[56:59], v[100:103]
	v_mfma_f32_16x16x32_f16 v[104:107], v[168:171], v[56:59], v[104:107]
	v_mfma_f32_16x16x32_f16 v[108:111], v[172:175], v[56:59], v[108:111]
	v_mul_f32_e32 v189, 0x3fb8aa3b, v189
	s_cmp_lt_u32 s42, 0
	s_cbranch_scc1 .Lmy_s2_kend2
	s_cmp_eq_u32 s42, 0
	s_cbranch_scc1 .Lmy_s2_diag3
	ds_read_b128 v[224:227], v38 offset:49792
	ds_read_b128 v[228:231], v38 offset:49808
	ds_read_b32 v232, v38 offset:49280
	ds_read_b128 v[160:163], v17 offset:0
	ds_read_b128 v[164:167], v17 offset:4096
	ds_read_b128 v[168:171], v17 offset:8192
	ds_read_b128 v[172:175], v17 offset:12288
	s_waitcnt lgkmcnt(7)
	v_fma_f32 v188, v188, s51, v189
	v_exp_f32_e32 v188, v188
	s_nop 0
	v_pk_mul_f32 v[176:177], v[176:177], v[188:189] op_sel_hi:[1,0]
	v_pk_mul_f32 v[178:179], v[178:179], v[188:189] op_sel_hi:[1,0]
	v_pk_mul_f32 v[180:181], v[180:181], v[188:189] op_sel_hi:[1,0]
	v_pk_mul_f32 v[182:183], v[182:183], v[188:189] op_sel_hi:[1,0]
	v_pk_mul_f32 v[176:177], v[60:61], v[176:177]
	v_pk_mul_f32 v[178:179], v[62:63], v[178:179]
	v_pk_mul_f32 v[180:181], v[64:65], v[180:181]
	v_pk_mul_f32 v[182:183], v[66:67], v[182:183]
	v_cvt_pk_f16_f32 v184, v176, v177
	v_cvt_pk_f16_f32 v185, v178, v179
	v_cvt_pk_f16_f32 v186, v180, v181
	v_cvt_pk_f16_f32 v187, v182, v183
	s_nop 1
	v_mfma_f32_16x16x32_f16 v[112:115], v[144:147], v[184:187], 0
	v_mfma_f32_16x16x32_f16 v[116:119], v[148:151], v[184:187], 0
	v_mfma_f32_16x16x32_f16 v[120:123], v[152:155], v[184:187], 0
	v_mfma_f32_16x16x32_f16 v[124:127], v[156:159], v[184:187], 0
	s_branch .Lmy_s2_knext4

.Lmy_s2_knext10:
.Lmy_s2_kend2:
	v_readlane_b32 s46, v11, s49
	v_readlane_b32 s47, v12, s49
	v_exp_f32_e32 v190, v189
	s_waitcnt lgkmcnt(0)
	s_nop 7
	v_cvt_f32_f16_e32 v198, v234
	v_cvt_f32_f16_sdwa v199, v234 dst_sel:DWORD dst_unused:UNUSED_PAD src0_sel:WORD_1
	v_cvt_f32_f16_e32 v200, v235
	v_cvt_f32_f16_sdwa v201, v235 dst_sel:DWORD dst_unused:UNUSED_PAD src0_sel:WORD_1
	v_pk_fma_f32 v[192:193], v[190:191], v[96:97], v[112:113] op_sel_hi:[0,1,1]
	v_pk_fma_f32 v[194:195], v[190:191], v[98:99], v[114:115] op_sel_hi:[0,1,1]
	v_pk_mul_f32 v[192:193], v[192:193], s[46:47] op_sel:[0,1] op_sel_hi:[1,1]
	v_pk_mul_f32 v[194:195], v[194:195], s[46:47] op_sel:[0,1] op_sel_hi:[1,1]
	v_pk_fma_f32 v[192:193], s[46:47], v[128:129], v[192:193] op_sel_hi:[0,1,1]
	v_pk_fma_f32 v[194:195], s[46:47], v[130:131], v[194:195] op_sel_hi:[0,1,1]
	v_pk_mul_f32 v[192:193], v[192:193], v[198:199]
	v_pk_mul_f32 v[194:195], v[194:195], v[200:201]
	v_pk_fma_f32 v[250:251], v[192:193], v[192:193], v[250:251]
	v_pk_fma_f32 v[250:251], v[194:195], v[194:195], v[250:251]
	v_cvt_pk_f16_f32 v196, v192, v193
	v_cvt_pk_f16_f32 v197, v194, v195
	global_store_dwordx2 v242, v[196:197], s[38:39]
	v_cvt_f32_f16_e32 v198, v236
	v_cvt_f32_f16_sdwa v199, v236 dst_sel:DWORD dst_unused:UNUSED_PAD src0_sel:WORD_1
	v_cvt_f32_f16_e32 v200, v237
	v_cvt_f32_f16_sdwa v201, v237 dst_sel:DWORD dst_unused:UNUSED_PAD src0_sel:WORD_1
	v_pk_fma_f32 v[192:193], v[190:191], v[100:101], v[116:117] op_sel_hi:[0,1,1]
	v_pk_fma_f32 v[194:195], v[190:191], v[102:103], v[118:119] op_sel_hi:[0,1,1]
	v_pk_mul_f32 v[192:193], v[192:193], s[46:47] op_sel:[0,1] op_sel_hi:[1,1]
	v_pk_mul_f32 v[194:195], v[194:195], s[46:47] op_sel:[0,1] op_sel_hi:[1,1]
	v_pk_fma_f32 v[192:193], s[46:47], v[132:133], v[192:193] op_sel_hi:[0,1,1]
	v_pk_fma_f32 v[194:195], s[46:47], v[134:135], v[194:195] op_sel_hi:[0,1,1]
	v_pk_mul_f32 v[192:193], v[192:193], v[198:199]
	v_pk_mul_f32 v[194:195], v[194:195], v[200:201]
	v_pk_fma_f32 v[250:251], v[192:193], v[192:193], v[250:251]
	v_pk_fma_f32 v[250:251], v[194:195], v[194:195], v[250:251]
	v_cvt_pk_f16_f32 v196, v192, v193
	v_cvt_pk_f16_f32 v197, v194, v195
	global_store_dwordx2 v242, v[196:197], s[38:39] offset:32
	v_cvt_f32_f16_e32 v198, v238
	v_cvt_f32_f16_sdwa v199, v238 dst_sel:DWORD dst_unused:UNUSED_PAD src0_sel:WORD_1
	v_cvt_f32_f16_e32 v200, v239
	v_cvt_f32_f16_sdwa v201, v239 dst_sel:DWORD dst_unused:UNUSED_PAD src0_sel:WORD_1
	v_pk_fma_f32 v[192:193], v[190:191], v[104:105], v[120:121] op_sel_hi:[0,1,1]
	v_pk_fma_f32 v[194:195], v[190:191], v[106:107], v[122:123] op_sel_hi:[0,1,1]
	v_pk_mul_f32 v[192:193], v[192:193], s[46:47] op_sel:[0,1] op_sel_hi:[1,1]
	v_pk_mul_f32 v[194:195], v[194:195], s[46:47] op_sel:[0,1] op_sel_hi:[1,1]
	v_pk_fma_f32 v[192:193], s[46:47], v[136:137], v[192:193] op_sel_hi:[0,1,1]
	v_pk_fma_f32 v[194:195], s[46:47], v[138:139], v[194:195] op_sel_hi:[0,1,1]
	v_pk_mul_f32 v[192:193], v[192:193], v[198:199]
	v_pk_mul_f32 v[194:195], v[194:195], v[200:201]
	v_pk_fma_f32 v[250:251], v[192:193], v[192:193], v[250:251]
	v_pk_fma_f32 v[250:251], v[194:195], v[194:195], v[250:251]
	v_cvt_pk_f16_f32 v196, v192, v193
	v_cvt_pk_f16_f32 v197, v194, v195
	global_store_dwordx2 v242, v[196:197], s[38:39] offset:64
	v_cvt_f32_f16_e32 v198, v240
	v_cvt_f32_f16_sdwa v199, v240 dst_sel:DWORD dst_unused:UNUSED_PAD src0_sel:WORD_1
	v_cvt_f32_f16_e32 v200, v241
	v_cvt_f32_f16_sdwa v201, v241 dst_sel:DWORD dst_unused:UNUSED_PAD src0_sel:WORD_1
	v_pk_fma_f32 v[192:193], v[190:191], v[108:109], v[124:125] op_sel_hi:[0,1,1]
	v_pk_fma_f32 v[194:195], v[190:191], v[110:111], v[126:127] op_sel_hi:[0,1,1]
	v_pk_mul_f32 v[192:193], v[192:193], s[46:47] op_sel:[0,1] op_sel_hi:[1,1]
	v_pk_mul_f32 v[194:195], v[194:195], s[46:47] op_sel:[0,1] op_sel_hi:[1,1]
	v_pk_fma_f32 v[192:193], s[46:47], v[140:141], v[192:193] op_sel_hi:[0,1,1]
	v_pk_fma_f32 v[194:195], s[46:47], v[142:143], v[194:195] op_sel_hi:[0,1,1]
	v_pk_mul_f32 v[192:193], v[192:193], v[198:199]
	v_pk_mul_f32 v[194:195], v[194:195], v[200:201]
	v_pk_fma_f32 v[250:251], v[192:193], v[192:193], v[250:251]
	v_pk_fma_f32 v[250:251], v[194:195], v[194:195], v[250:251]
	v_cvt_pk_f16_f32 v196, v192, v193
	v_cvt_pk_f16_f32 v197, v194, v195
	global_store_dwordx2 v242, v[196:197], s[38:39] offset:96
	s_add_u32 s38, s38, 0x80
	s_addc_u32 s39, s39, 0
	s_waitcnt vmcnt(11)
	s_add_u32 s49, s48, 1
	s_waitcnt lgkmcnt(0)
	s_barrier
	ds_read_b128 v[144:147], v20 offset:16384
	ds_read_b128 v[148:151], v20 offset:20480
	ds_read_b128 v[152:155], v20 offset:24576
	ds_read_b128 v[156:159], v20 offset:28672
	ds_read_b32 v189, v37 offset:49152
	s_add_u32 m0, s43, 0x0
	s_nop 0
	global_load_lds_dwordx4 v4, s[30:31]
	s_add_u32 m0, s43, 0x4000
	s_nop 0
	global_load_lds_dwordx4 v6, s[32:33]
	s_add_u32 m0, s43, 0x8000
	s_nop 0
	global_load_lds_dwordx4 v8, s[34:35]
	s_add_u32 m0, s43, 0x2000
	s_nop 0
	global_load_lds_dwordx4 v5, s[30:31]
	s_add_u32 m0, s43, 0x6000
	s_nop 0
	global_load_lds_dwordx4 v7, s[32:33]
	s_add_u32 m0, s43, 0xa000
	s_nop 0
	global_load_lds_dwordx4 v9, s[34:35]
	s_add_u32 m0, s44, 0xc000
	s_nop 0
	global_load_lds_dword v10, s[36:37]
	s_add_u32 s30, s30, 0x80000
	s_addc_u32 s31, s31, 0
	s_add_u32 s32, s32, 0x4000
	s_addc_u32 s33, s33, 0
	s_add_u32 s34, s34, 0x80
	s_addc_u32 s35, s35, 0
	s_add_u32 s36, s36, 0x4000
	s_addc_u32 s37, s37, 0
	ds_read_b128 v[160:163], v21 offset:16384
	ds_read_b128 v[164:167], v21 offset:20480
	ds_read_b128 v[168:171], v21 offset:24576
	ds_read_b128 v[172:175], v21 offset:28672
	s_waitcnt lgkmcnt(4)
	v_mfma_f32_16x16x32_f16 v[96:99], v[144:147], v[44:47], 0
	v_mfma_f32_16x16x32_f16 v[100:103], v[148:151], v[44:47], 0
	v_mfma_f32_16x16x32_f16 v[104:107], v[152:155], v[44:47], 0
	v_mfma_f32_16x16x32_f16 v[108:111], v[156:159], v[44:47], 0
	ds_read_b128 v[144:147], v22 offset:16384
	ds_read_b128 v[148:151], v22 offset:20480
	ds_read_b128 v[152:155], v22 offset:24576
	ds_read_b128 v[156:159], v22 offset:28672
	s_waitcnt lgkmcnt(4)
	v_mfma_f32_16x16x32_f16 v[96:99], v[160:163], v[48:51], v[96:99]
	v_mfma_f32_16x16x32_f16 v[100:103], v[164:167], v[48:51], v[100:103]
	v_mfma_f32_16x16x32_f16 v[104:107], v[168:171], v[48:51], v[104:107]
	v_mfma_f32_16x16x32_f16 v[108:111], v[172:175], v[48:51], v[108:111]
	ds_read_b128 v[160:163], v23 offset:16384
	ds_read_b128 v[164:167], v23 offset:20480
	ds_read_b128 v[168:171], v23 offset:24576
	ds_read_b128 v[172:175], v23 offset:28672
	s_waitcnt lgkmcnt(4)
	v_mfma_f32_16x16x32_f16 v[96:99], v[144:147], v[52:55], v[96:99]
	v_mfma_f32_16x16x32_f16 v[100:103], v[148:151], v[52:55], v[100:103]
	v_mfma_f32_16x16x32_f16 v[104:107], v[152:155], v[52:55], v[104:107]
	v_mfma_f32_16x16x32_f16 v[108:111], v[156:159], v[52:55], v[108:111]
	ds_read_b128 v[176:179], v39 offset:49664
	ds_read_b128 v[180:183], v39 offset:49680
	ds_read_b32 v188, v39 offset:49152
	ds_read_b128 v[144:147], v20 offset:0
	ds_read_b128 v[148:151], v20 offset:4096
	ds_read_b128 v[152:155], v20 offset:8192
	ds_read_b128 v[156:159], v20 offset:12288
	s_waitcnt lgkmcnt(7)
	v_mfma_f32_16x16x32_f16 v[96:99], v[160:163], v[56:59], v[96:99]
	v_mfma_f32_16x16x32_f16 v[100:103], v[164:167], v[56:59], v[100:103]
	v_mfma_f32_16x16x32_f16 v[104:107], v[168:171], v[56:59], v[104:107]
	v_mfma_f32_16x16x32_f16 v[108:111], v[172:175], v[56:59], v[108:111]
	v_mul_f32_e32 v189, 0x3fb8aa3b, v189
	s_cmp_lt_u32 s42, 0
	s_cbranch_scc1 .Lmy_s2_kend11
	s_cmp_eq_u32 s42, 0
	s_cbranch_scc1 .Lmy_s2_diag12
	ds_read_b128 v[224:227], v39 offset:49792
	ds_read_b128 v[228:231], v39 offset:49808
	ds_read_b32 v232, v39 offset:49280
	ds_read_b128 v[160:163], v21 offset:0
	ds_read_b128 v[164:167], v21 offset:4096
	ds_read_b128 v[168:171], v21 offset:8192
	ds_read_b128 v[172:175], v21 offset:12288
	s_waitcnt lgkmcnt(7)
	v_fma_f32 v188, v188, s51, v189
	v_exp_f32_e32 v188, v188
	s_nop 0
	v_pk_mul_f32 v[176:177], v[176:177], v[188:189] op_sel_hi:[1,0]
	v_pk_mul_f32 v[178:179], v[178:179], v[188:189] op_sel_hi:[1,0]
	v_pk_mul_f32 v[180:181], v[180:181], v[188:189] op_sel_hi:[1,0]
	v_pk_mul_f32 v[182:183], v[182:183], v[188:189] op_sel_hi:[1,0]
	v_pk_mul_f32 v[176:177], v[60:61], v[176:177]
	v_pk_mul_f32 v[178:179], v[62:63], v[178:179]
	v_pk_mul_f32 v[180:181], v[64:65], v[180:181]
	v_pk_mul_f32 v[182:183], v[66:67], v[182:183]
	v_cvt_pk_f16_f32 v184, v176, v177
	v_cvt_pk_f16_f32 v185, v178, v179
	v_cvt_pk_f16_f32 v186, v180, v181
	v_cvt_pk_f16_f32 v187, v182, v183
	s_nop 1
	v_mfma_f32_16x16x32_f16 v[112:115], v[144:147], v[184:187], 0
	v_mfma_f32_16x16x32_f16 v[116:119], v[148:151], v[184:187], 0
	v_mfma_f32_16x16x32_f16 v[120:123], v[152:155], v[184:187], 0
	v_mfma_f32_16x16x32_f16 v[124:127], v[156:159], v[184:187], 0
	s_branch .Lmy_s2_knext13

.Lmy_s2_knext19:
.Lmy_s2_kend11:
	v_readlane_b32 s46, v11, s49
	v_readlane_b32 s47, v12, s49
	v_exp_f32_e32 v190, v189
	s_waitcnt lgkmcnt(0)
	s_nop 7
	v_cvt_f32_f16_e32 v198, v234
	v_cvt_f32_f16_sdwa v199, v234 dst_sel:DWORD dst_unused:UNUSED_PAD src0_sel:WORD_1
	v_cvt_f32_f16_e32 v200, v235
	v_cvt_f32_f16_sdwa v201, v235 dst_sel:DWORD dst_unused:UNUSED_PAD src0_sel:WORD_1
	v_pk_fma_f32 v[192:193], v[190:191], v[96:97], v[112:113] op_sel_hi:[0,1,1]
	v_pk_fma_f32 v[194:195], v[190:191], v[98:99], v[114:115] op_sel_hi:[0,1,1]
	v_pk_mul_f32 v[192:193], v[192:193], s[46:47] op_sel:[0,1] op_sel_hi:[1,1]
	v_pk_mul_f32 v[194:195], v[194:195], s[46:47] op_sel:[0,1] op_sel_hi:[1,1]
	v_pk_fma_f32 v[192:193], s[46:47], v[128:129], v[192:193] op_sel_hi:[0,1,1]
	v_pk_fma_f32 v[194:195], s[46:47], v[130:131], v[194:195] op_sel_hi:[0,1,1]
	v_pk_mul_f32 v[192:193], v[192:193], v[198:199]
	v_pk_mul_f32 v[194:195], v[194:195], v[200:201]
	v_pk_fma_f32 v[250:251], v[192:193], v[192:193], v[250:251]
	v_pk_fma_f32 v[250:251], v[194:195], v[194:195], v[250:251]
	v_cvt_pk_f16_f32 v196, v192, v193
	v_cvt_pk_f16_f32 v197, v194, v195
	global_store_dwordx2 v242, v[196:197], s[38:39]
	v_cvt_f32_f16_e32 v198, v236
	v_cvt_f32_f16_sdwa v199, v236 dst_sel:DWORD dst_unused:UNUSED_PAD src0_sel:WORD_1
	v_cvt_f32_f16_e32 v200, v237
	v_cvt_f32_f16_sdwa v201, v237 dst_sel:DWORD dst_unused:UNUSED_PAD src0_sel:WORD_1
	v_pk_fma_f32 v[192:193], v[190:191], v[100:101], v[116:117] op_sel_hi:[0,1,1]
	v_pk_fma_f32 v[194:195], v[190:191], v[102:103], v[118:119] op_sel_hi:[0,1,1]
	v_pk_mul_f32 v[192:193], v[192:193], s[46:47] op_sel:[0,1] op_sel_hi:[1,1]
	v_pk_mul_f32 v[194:195], v[194:195], s[46:47] op_sel:[0,1] op_sel_hi:[1,1]
	v_pk_fma_f32 v[192:193], s[46:47], v[132:133], v[192:193] op_sel_hi:[0,1,1]
	v_pk_fma_f32 v[194:195], s[46:47], v[134:135], v[194:195] op_sel_hi:[0,1,1]
	v_pk_mul_f32 v[192:193], v[192:193], v[198:199]
	v_pk_mul_f32 v[194:195], v[194:195], v[200:201]
	v_pk_fma_f32 v[250:251], v[192:193], v[192:193], v[250:251]
	v_pk_fma_f32 v[250:251], v[194:195], v[194:195], v[250:251]
	v_cvt_pk_f16_f32 v196, v192, v193
	v_cvt_pk_f16_f32 v197, v194, v195
	global_store_dwordx2 v242, v[196:197], s[38:39] offset:32
	v_cvt_f32_f16_e32 v198, v238
	v_cvt_f32_f16_sdwa v199, v238 dst_sel:DWORD dst_unused:UNUSED_PAD src0_sel:WORD_1
	v_cvt_f32_f16_e32 v200, v239
	v_cvt_f32_f16_sdwa v201, v239 dst_sel:DWORD dst_unused:UNUSED_PAD src0_sel:WORD_1
	v_pk_fma_f32 v[192:193], v[190:191], v[104:105], v[120:121] op_sel_hi:[0,1,1]
	v_pk_fma_f32 v[194:195], v[190:191], v[106:107], v[122:123] op_sel_hi:[0,1,1]
	v_pk_mul_f32 v[192:193], v[192:193], s[46:47] op_sel:[0,1] op_sel_hi:[1,1]
	v_pk_mul_f32 v[194:195], v[194:195], s[46:47] op_sel:[0,1] op_sel_hi:[1,1]
	v_pk_fma_f32 v[192:193], s[46:47], v[136:137], v[192:193] op_sel_hi:[0,1,1]
	v_pk_fma_f32 v[194:195], s[46:47], v[138:139], v[194:195] op_sel_hi:[0,1,1]
	v_pk_mul_f32 v[192:193], v[192:193], v[198:199]
	v_pk_mul_f32 v[194:195], v[194:195], v[200:201]
	v_pk_fma_f32 v[250:251], v[192:193], v[192:193], v[250:251]
	v_pk_fma_f32 v[250:251], v[194:195], v[194:195], v[250:251]
	v_cvt_pk_f16_f32 v196, v192, v193
	v_cvt_pk_f16_f32 v197, v194, v195
	global_store_dwordx2 v242, v[196:197], s[38:39] offset:64
	v_cvt_f32_f16_e32 v198, v240
	v_cvt_f32_f16_sdwa v199, v240 dst_sel:DWORD dst_unused:UNUSED_PAD src0_sel:WORD_1
	v_cvt_f32_f16_e32 v200, v241
	v_cvt_f32_f16_sdwa v201, v241 dst_sel:DWORD dst_unused:UNUSED_PAD src0_sel:WORD_1
	v_pk_fma_f32 v[192:193], v[190:191], v[108:109], v[124:125] op_sel_hi:[0,1,1]
	v_pk_fma_f32 v[194:195], v[190:191], v[110:111], v[126:127] op_sel_hi:[0,1,1]
	v_pk_mul_f32 v[192:193], v[192:193], s[46:47] op_sel:[0,1] op_sel_hi:[1,1]
	v_pk_mul_f32 v[194:195], v[194:195], s[46:47] op_sel:[0,1] op_sel_hi:[1,1]
	v_pk_fma_f32 v[192:193], s[46:47], v[140:141], v[192:193] op_sel_hi:[0,1,1]
	v_pk_fma_f32 v[194:195], s[46:47], v[142:143], v[194:195] op_sel_hi:[0,1,1]
	v_pk_mul_f32 v[192:193], v[192:193], v[198:199]
	v_pk_mul_f32 v[194:195], v[194:195], v[200:201]
	v_pk_fma_f32 v[250:251], v[192:193], v[192:193], v[250:251]
	v_pk_fma_f32 v[250:251], v[194:195], v[194:195], v[250:251]
	v_cvt_pk_f16_f32 v196, v192, v193
	v_cvt_pk_f16_f32 v197, v194, v195
	global_store_dwordx2 v242, v[196:197], s[38:39] offset:96
	s_add_u32 s38, s38, 0x80
	s_addc_u32 s39, s39, 0
	s_waitcnt vmcnt(15)
	s_add_u32 s49, s48, 2
	s_waitcnt lgkmcnt(0)
	s_barrier
	ds_read_b128 v[144:147], v212 offset:16384
	ds_read_b128 v[148:151], v212 offset:20480
	ds_read_b128 v[152:155], v212 offset:24576
	ds_read_b128 v[156:159], v212 offset:28672
	ds_read_b32 v189, v220 offset:49152
	s_add_u32 m0, s43, 0xc800
	s_nop 0
	global_load_lds_dwordx4 v4, s[30:31]
	s_add_u32 m0, s43, 0x10800
	s_nop 0
	global_load_lds_dwordx4 v6, s[32:33]
	s_add_u32 m0, s43, 0x14800
	s_nop 0
	global_load_lds_dwordx4 v8, s[34:35]
	s_add_u32 m0, s43, 0xe800
	s_nop 0
	global_load_lds_dwordx4 v5, s[30:31]
	s_add_u32 m0, s43, 0x12800
	s_nop 0
	global_load_lds_dwordx4 v7, s[32:33]
	s_add_u32 m0, s43, 0x16800
	s_nop 0
	global_load_lds_dwordx4 v9, s[34:35]
	s_add_u32 m0, s44, 0x18800
	s_nop 0
	global_load_lds_dword v10, s[36:37]
	s_add_u32 s30, s30, 0x80000
	s_addc_u32 s31, s31, 0
	s_add_u32 s32, s32, 0x4000
	s_addc_u32 s33, s33, 0
	s_add_u32 s34, s34, 0x80
	s_addc_u32 s35, s35, 0
	s_add_u32 s36, s36, 0x4000
	s_addc_u32 s37, s37, 0
	ds_read_b128 v[160:163], v213 offset:16384
	ds_read_b128 v[164:167], v213 offset:20480
	ds_read_b128 v[168:171], v213 offset:24576
	ds_read_b128 v[172:175], v213 offset:28672
	s_waitcnt lgkmcnt(4)
	v_mfma_f32_16x16x32_f16 v[96:99], v[144:147], v[44:47], 0
	v_mfma_f32_16x16x32_f16 v[100:103], v[148:151], v[44:47], 0
	v_mfma_f32_16x16x32_f16 v[104:107], v[152:155], v[44:47], 0
	v_mfma_f32_16x16x32_f16 v[108:111], v[156:159], v[44:47], 0
	ds_read_b128 v[144:147], v214 offset:16384
	ds_read_b128 v[148:151], v214 offset:20480
	ds_read_b128 v[152:155], v214 offset:24576
	ds_read_b128 v[156:159], v214 offset:28672
	s_waitcnt lgkmcnt(4)
	v_mfma_f32_16x16x32_f16 v[96:99], v[160:163], v[48:51], v[96:99]
	v_mfma_f32_16x16x32_f16 v[100:103], v[164:167], v[48:51], v[100:103]
	v_mfma_f32_16x16x32_f16 v[104:107], v[168:171], v[48:51], v[104:107]
	v_mfma_f32_16x16x32_f16 v[108:111], v[172:175], v[48:51], v[108:111]
	ds_read_b128 v[160:163], v215 offset:16384
	ds_read_b128 v[164:167], v215 offset:20480
	ds_read_b128 v[168:171], v215 offset:24576
	ds_read_b128 v[172:175], v215 offset:28672
	s_waitcnt lgkmcnt(4)
	v_mfma_f32_16x16x32_f16 v[96:99], v[144:147], v[52:55], v[96:99]
	v_mfma_f32_16x16x32_f16 v[100:103], v[148:151], v[52:55], v[100:103]
	v_mfma_f32_16x16x32_f16 v[104:107], v[152:155], v[52:55], v[104:107]
	v_mfma_f32_16x16x32_f16 v[108:111], v[156:159], v[52:55], v[108:111]
	ds_read_b128 v[176:179], v221 offset:49664
	ds_read_b128 v[180:183], v221 offset:49680
	ds_read_b32 v188, v221 offset:49152
	ds_read_b128 v[144:147], v212 offset:0
	ds_read_b128 v[148:151], v212 offset:4096
	ds_read_b128 v[152:155], v212 offset:8192
	ds_read_b128 v[156:159], v212 offset:12288
	s_waitcnt lgkmcnt(7)
	v_mfma_f32_16x16x32_f16 v[96:99], v[160:163], v[56:59], v[96:99]
	v_mfma_f32_16x16x32_f16 v[100:103], v[164:167], v[56:59], v[100:103]
	v_mfma_f32_16x16x32_f16 v[104:107], v[168:171], v[56:59], v[104:107]
	v_mfma_f32_16x16x32_f16 v[108:111], v[172:175], v[56:59], v[108:111]
	v_mul_f32_e32 v189, 0x3fb8aa3b, v189
	s_cmp_lt_u32 s42, 0
	s_cbranch_scc1 .Lmy_s2_kend20
	s_cmp_eq_u32 s42, 0
	s_cbranch_scc1 .Lmy_s2_diag21
	ds_read_b128 v[224:227], v221 offset:49792
	ds_read_b128 v[228:231], v221 offset:49808
	ds_read_b32 v232, v221 offset:49280
	ds_read_b128 v[160:163], v213 offset:0
	ds_read_b128 v[164:167], v213 offset:4096
	ds_read_b128 v[168:171], v213 offset:8192
	ds_read_b128 v[172:175], v213 offset:12288
	s_waitcnt lgkmcnt(7)
	v_fma_f32 v188, v188, s51, v189
	v_exp_f32_e32 v188, v188
	s_nop 0
	v_pk_mul_f32 v[176:177], v[176:177], v[188:189] op_sel_hi:[1,0]
	v_pk_mul_f32 v[178:179], v[178:179], v[188:189] op_sel_hi:[1,0]
	v_pk_mul_f32 v[180:181], v[180:181], v[188:189] op_sel_hi:[1,0]
	v_pk_mul_f32 v[182:183], v[182:183], v[188:189] op_sel_hi:[1,0]
	v_pk_mul_f32 v[176:177], v[60:61], v[176:177]
	v_pk_mul_f32 v[178:179], v[62:63], v[178:179]
	v_pk_mul_f32 v[180:181], v[64:65], v[180:181]
	v_pk_mul_f32 v[182:183], v[66:67], v[182:183]
	v_cvt_pk_f16_f32 v184, v176, v177
	v_cvt_pk_f16_f32 v185, v178, v179
	v_cvt_pk_f16_f32 v186, v180, v181
	v_cvt_pk_f16_f32 v187, v182, v183
	s_nop 1
	v_mfma_f32_16x16x32_f16 v[112:115], v[144:147], v[184:187], 0
	v_mfma_f32_16x16x32_f16 v[116:119], v[148:151], v[184:187], 0
	v_mfma_f32_16x16x32_f16 v[120:123], v[152:155], v[184:187], 0
	v_mfma_f32_16x16x32_f16 v[124:127], v[156:159], v[184:187], 0
	s_branch .Lmy_s2_knext22

.Lmy_s2_knext28:
.Lmy_s2_kend20:
	v_readlane_b32 s46, v11, s49
	v_readlane_b32 s47, v12, s49
	v_exp_f32_e32 v190, v189
	s_waitcnt lgkmcnt(0)
	s_nop 7
	v_cvt_f32_f16_e32 v198, v234
	v_cvt_f32_f16_sdwa v199, v234 dst_sel:DWORD dst_unused:UNUSED_PAD src0_sel:WORD_1
	v_cvt_f32_f16_e32 v200, v235
	v_cvt_f32_f16_sdwa v201, v235 dst_sel:DWORD dst_unused:UNUSED_PAD src0_sel:WORD_1
	v_pk_fma_f32 v[192:193], v[190:191], v[96:97], v[112:113] op_sel_hi:[0,1,1]
	v_pk_fma_f32 v[194:195], v[190:191], v[98:99], v[114:115] op_sel_hi:[0,1,1]
	v_pk_mul_f32 v[192:193], v[192:193], s[46:47] op_sel:[0,1] op_sel_hi:[1,1]
	v_pk_mul_f32 v[194:195], v[194:195], s[46:47] op_sel:[0,1] op_sel_hi:[1,1]
	v_pk_fma_f32 v[192:193], s[46:47], v[128:129], v[192:193] op_sel_hi:[0,1,1]
	v_pk_fma_f32 v[194:195], s[46:47], v[130:131], v[194:195] op_sel_hi:[0,1,1]
	v_pk_mul_f32 v[192:193], v[192:193], v[198:199]
	v_pk_mul_f32 v[194:195], v[194:195], v[200:201]
	v_pk_fma_f32 v[250:251], v[192:193], v[192:193], v[250:251]
	v_pk_fma_f32 v[250:251], v[194:195], v[194:195], v[250:251]
	v_cvt_pk_f16_f32 v196, v192, v193
	v_cvt_pk_f16_f32 v197, v194, v195
	global_store_dwordx2 v242, v[196:197], s[38:39]
	v_cvt_f32_f16_e32 v198, v236
	v_cvt_f32_f16_sdwa v199, v236 dst_sel:DWORD dst_unused:UNUSED_PAD src0_sel:WORD_1
	v_cvt_f32_f16_e32 v200, v237
	v_cvt_f32_f16_sdwa v201, v237 dst_sel:DWORD dst_unused:UNUSED_PAD src0_sel:WORD_1
	v_pk_fma_f32 v[192:193], v[190:191], v[100:101], v[116:117] op_sel_hi:[0,1,1]
	v_pk_fma_f32 v[194:195], v[190:191], v[102:103], v[118:119] op_sel_hi:[0,1,1]
	v_pk_mul_f32 v[192:193], v[192:193], s[46:47] op_sel:[0,1] op_sel_hi:[1,1]
	v_pk_mul_f32 v[194:195], v[194:195], s[46:47] op_sel:[0,1] op_sel_hi:[1,1]
	v_pk_fma_f32 v[192:193], s[46:47], v[132:133], v[192:193] op_sel_hi:[0,1,1]
	v_pk_fma_f32 v[194:195], s[46:47], v[134:135], v[194:195] op_sel_hi:[0,1,1]
	v_pk_mul_f32 v[192:193], v[192:193], v[198:199]
	v_pk_mul_f32 v[194:195], v[194:195], v[200:201]
	v_pk_fma_f32 v[250:251], v[192:193], v[192:193], v[250:251]
	v_pk_fma_f32 v[250:251], v[194:195], v[194:195], v[250:251]
	v_cvt_pk_f16_f32 v196, v192, v193
	v_cvt_pk_f16_f32 v197, v194, v195
	global_store_dwordx2 v242, v[196:197], s[38:39] offset:32
	v_cvt_f32_f16_e32 v198, v238
	v_cvt_f32_f16_sdwa v199, v238 dst_sel:DWORD dst_unused:UNUSED_PAD src0_sel:WORD_1
	v_cvt_f32_f16_e32 v200, v239
	v_cvt_f32_f16_sdwa v201, v239 dst_sel:DWORD dst_unused:UNUSED_PAD src0_sel:WORD_1
	v_pk_fma_f32 v[192:193], v[190:191], v[104:105], v[120:121] op_sel_hi:[0,1,1]
	v_pk_fma_f32 v[194:195], v[190:191], v[106:107], v[122:123] op_sel_hi:[0,1,1]
	v_pk_mul_f32 v[192:193], v[192:193], s[46:47] op_sel:[0,1] op_sel_hi:[1,1]
	v_pk_mul_f32 v[194:195], v[194:195], s[46:47] op_sel:[0,1] op_sel_hi:[1,1]
	v_pk_fma_f32 v[192:193], s[46:47], v[136:137], v[192:193] op_sel_hi:[0,1,1]
	v_pk_fma_f32 v[194:195], s[46:47], v[138:139], v[194:195] op_sel_hi:[0,1,1]
	v_pk_mul_f32 v[192:193], v[192:193], v[198:199]
	v_pk_mul_f32 v[194:195], v[194:195], v[200:201]
	v_pk_fma_f32 v[250:251], v[192:193], v[192:193], v[250:251]
	v_pk_fma_f32 v[250:251], v[194:195], v[194:195], v[250:251]
	v_cvt_pk_f16_f32 v196, v192, v193
	v_cvt_pk_f16_f32 v197, v194, v195
	global_store_dwordx2 v242, v[196:197], s[38:39] offset:64
	v_cvt_f32_f16_e32 v198, v240
	v_cvt_f32_f16_sdwa v199, v240 dst_sel:DWORD dst_unused:UNUSED_PAD src0_sel:WORD_1
	v_cvt_f32_f16_e32 v200, v241
	v_cvt_f32_f16_sdwa v201, v241 dst_sel:DWORD dst_unused:UNUSED_PAD src0_sel:WORD_1
	v_pk_fma_f32 v[192:193], v[190:191], v[108:109], v[124:125] op_sel_hi:[0,1,1]
	v_pk_fma_f32 v[194:195], v[190:191], v[110:111], v[126:127] op_sel_hi:[0,1,1]
	v_pk_mul_f32 v[192:193], v[192:193], s[46:47] op_sel:[0,1] op_sel_hi:[1,1]
	v_pk_mul_f32 v[194:195], v[194:195], s[46:47] op_sel:[0,1] op_sel_hi:[1,1]
	v_pk_fma_f32 v[192:193], s[46:47], v[140:141], v[192:193] op_sel_hi:[0,1,1]
	v_pk_fma_f32 v[194:195], s[46:47], v[142:143], v[194:195] op_sel_hi:[0,1,1]
	v_pk_mul_f32 v[192:193], v[192:193], v[198:199]
	v_pk_mul_f32 v[194:195], v[194:195], v[200:201]
	v_pk_fma_f32 v[250:251], v[192:193], v[192:193], v[250:251]
	v_pk_fma_f32 v[250:251], v[194:195], v[194:195], v[250:251]
	v_cvt_pk_f16_f32 v196, v192, v193
	v_cvt_pk_f16_f32 v197, v194, v195
	global_store_dwordx2 v242, v[196:197], s[38:39] offset:96
	s_add_u32 s38, s38, 0x80
	s_addc_u32 s39, s39, 0
	s_add_u32 s48, s48, 3
	s_cmp_lt_u32 s48, 6
	s_cbranch_scc1 .Lmy_s2_heads1
	s_waitcnt vmcnt(15)
	s_waitcnt lgkmcnt(0)
	s_barrier
	ds_read_b128 v[144:147], v16 offset:16384
	ds_read_b128 v[148:151], v16 offset:20480
	ds_read_b128 v[152:155], v16 offset:24576
	ds_read_b128 v[156:159], v16 offset:28672
	ds_read_b32 v189, v36 offset:49152
	ds_read_b128 v[160:163], v17 offset:16384
	ds_read_b128 v[164:167], v17 offset:20480
	ds_read_b128 v[168:171], v17 offset:24576
	ds_read_b128 v[172:175], v17 offset:28672
	s_waitcnt lgkmcnt(4)
	v_mfma_f32_16x16x32_f16 v[96:99], v[144:147], v[44:47], 0
	v_mfma_f32_16x16x32_f16 v[100:103], v[148:151], v[44:47], 0
	v_mfma_f32_16x16x32_f16 v[104:107], v[152:155], v[44:47], 0
	v_mfma_f32_16x16x32_f16 v[108:111], v[156:159], v[44:47], 0
	ds_read_b128 v[144:147], v18 offset:16384
	ds_read_b128 v[148:151], v18 offset:20480
	ds_read_b128 v[152:155], v18 offset:24576
	ds_read_b128 v[156:159], v18 offset:28672
	s_waitcnt lgkmcnt(4)
	v_mfma_f32_16x16x32_f16 v[96:99], v[160:163], v[48:51], v[96:99]
	v_mfma_f32_16x16x32_f16 v[100:103], v[164:167], v[48:51], v[100:103]
	v_mfma_f32_16x16x32_f16 v[104:107], v[168:171], v[48:51], v[104:107]
	v_mfma_f32_16x16x32_f16 v[108:111], v[172:175], v[48:51], v[108:111]
	ds_read_b128 v[160:163], v19 offset:16384
	ds_read_b128 v[164:167], v19 offset:20480
	ds_read_b128 v[168:171], v19 offset:24576
	ds_read_b128 v[172:175], v19 offset:28672
	s_waitcnt lgkmcnt(4)
	v_mfma_f32_16x16x32_f16 v[96:99], v[144:147], v[52:55], v[96:99]
	v_mfma_f32_16x16x32_f16 v[100:103], v[148:151], v[52:55], v[100:103]
	v_mfma_f32_16x16x32_f16 v[104:107], v[152:155], v[52:55], v[104:107]
	v_mfma_f32_16x16x32_f16 v[108:111], v[156:159], v[52:55], v[108:111]
	ds_read_b128 v[176:179], v38 offset:49664
	ds_read_b128 v[180:183], v38 offset:49680
	ds_read_b32 v188, v38 offset:49152
	ds_read_b128 v[144:147], v16 offset:0
	ds_read_b128 v[148:151], v16 offset:4096
	ds_read_b128 v[152:155], v16 offset:8192
	ds_read_b128 v[156:159], v16 offset:12288
	s_waitcnt lgkmcnt(7)
	v_mfma_f32_16x16x32_f16 v[96:99], v[160:163], v[56:59], v[96:99]
	v_mfma_f32_16x16x32_f16 v[100:103], v[164:167], v[56:59], v[100:103]
	v_mfma_f32_16x16x32_f16 v[104:107], v[168:171], v[56:59], v[104:107]
	v_mfma_f32_16x16x32_f16 v[108:111], v[172:175], v[56:59], v[108:111]
	v_mul_f32_e32 v189, 0x3fb8aa3b, v189
	s_cmp_lt_u32 s42, 0
	s_cbranch_scc1 .Lmy_s2_kend29
	s_cmp_eq_u32 s42, 0
	s_cbranch_scc1 .Lmy_s2_diag30
	ds_read_b128 v[224:227], v38 offset:49792
	ds_read_b128 v[228:231], v38 offset:49808
	ds_read_b32 v232, v38 offset:49280
	ds_read_b128 v[160:163], v17 offset:0
	ds_read_b128 v[164:167], v17 offset:4096
	ds_read_b128 v[168:171], v17 offset:8192
	ds_read_b128 v[172:175], v17 offset:12288
	s_waitcnt lgkmcnt(7)
	v_fma_f32 v188, v188, s51, v189
	v_exp_f32_e32 v188, v188
	s_nop 0
	v_pk_mul_f32 v[176:177], v[176:177], v[188:189] op_sel_hi:[1,0]
	v_pk_mul_f32 v[178:179], v[178:179], v[188:189] op_sel_hi:[1,0]
	v_pk_mul_f32 v[180:181], v[180:181], v[188:189] op_sel_hi:[1,0]
	v_pk_mul_f32 v[182:183], v[182:183], v[188:189] op_sel_hi:[1,0]
	v_pk_mul_f32 v[176:177], v[60:61], v[176:177]
	v_pk_mul_f32 v[178:179], v[62:63], v[178:179]
	v_pk_mul_f32 v[180:181], v[64:65], v[180:181]
	v_pk_mul_f32 v[182:183], v[66:67], v[182:183]
	v_cvt_pk_f16_f32 v184, v176, v177
	v_cvt_pk_f16_f32 v185, v178, v179
	v_cvt_pk_f16_f32 v186, v180, v181
	v_cvt_pk_f16_f32 v187, v182, v183
	s_nop 1
	v_mfma_f32_16x16x32_f16 v[112:115], v[144:147], v[184:187], 0
	v_mfma_f32_16x16x32_f16 v[116:119], v[148:151], v[184:187], 0
	v_mfma_f32_16x16x32_f16 v[120:123], v[152:155], v[184:187], 0
	v_mfma_f32_16x16x32_f16 v[124:127], v[156:159], v[184:187], 0
	s_branch .Lmy_s2_knext31
